# plus DSA selection: candidate-list loops read one iteration ahead, private-list max via DPP/permlane
# speedup vs baseline: 1.0184x; 1.0068x over previous
; __device__ __forceinline__ int lane_op() { int l = (int)__builtin_amdgcn_mbcnt_hi(~0u, __builtin_amdgcn_mbcnt_lo(~0u, 0u)); asm volatile("" : "+v"(l)); return l; }
; #define SHX(v, m, l) bperm_((l) ^ (m), (v))
; __device__ __forceinline__ bool dsa2_sampled(LAS unsigned char* wl, const unsigned (&kk)[128], int nreg, int n, int lane) {
;     ...
;     int mxc = cur; { const int lq_ = lane_op();
; #pragma unroll
;         for (int o = 1; o < 64; o <<= 1) { const int t2 = SHX(mxc, o, lq_); mxc = t2 > mxc ? t2 : mxc; } }
;     mxc = __builtin_amdgcn_readfirstlane(mxc);
;     if (mxc > 24) return false;
;     int A = 0, C = 0;
; #pragma unroll 1
;     for (int s = 0; s < mxc; ++s) { const bool vld = s < cur; const unsigned long long e = vld ? PRIV[s * 64 + lane] : 0ull; const unsigned k = (unsigned)(e >> 32), ix = (unsigned)e;
.LBB0_1227:
	s_or_b64 exec, exec, s[0:1]
	v_mov_b32_e32 v0, v251
	s_waitcnt lgkmcnt(0)
	s_mov_b64 s[0:1], -1
	v_lshlrev_b32_e32 v0, 2, v0
	v_mov_b32_e32 v1, v3
	s_nop 1
	v_max_i32_dpp v1, v1, v1 quad_perm:[1,0,3,2] row_mask:0xf bank_mask:0xf
	s_nop 1
	v_max_i32_dpp v1, v1, v1 quad_perm:[2,3,0,1] row_mask:0xf bank_mask:0xf
	s_nop 1
	v_max_i32_dpp v1, v1, v1 row_half_mirror row_mask:0xf bank_mask:0xf
	s_nop 1
	v_max_i32_dpp v1, v1, v1 row_mirror row_mask:0xf bank_mask:0xf
	v_mov_b32_e32 v0, v1
	v_mov_b32_e32 v4, v1
	s_nop 1
	v_permlane16_swap_b32 v0, v4
	v_max_i32_e32 v1, v0, v4
	v_mov_b32_e32 v0, v1
	v_mov_b32_e32 v4, v1
	s_nop 1
	v_permlane32_swap_b32 v0, v4
	v_max_i32_e32 v0, v0, v4
	s_nop 0
	v_readfirstlane_b32 s12, v0
	s_cmp_gt_i32 s12, 24
	s_cbranch_scc1 .LBB0_1271
	s_mov_b32 s20, 0
	s_cmp_lt_i32 s12, 1
	s_cbranch_scc1 .LBB0_1246
	v_mov_b32_e32 v4, v6
	s_mov_b32 s21, 0
	s_mov_b32 s13, 0
	ds_read_b64 v[186:187], v4
	s_branch .LBB0_1231

; __device__ __forceinline__ bool dsa2_sampled(LAS unsigned char* wl, const unsigned (&kk)[128], int nreg, int n, int lane) {
;     ...
;     for (int s = 0; s < mxc; ++s) { const bool vld = s < cur; const unsigned long long e = vld ? PRIV[s * 64 + lane] : 0ull; const unsigned k = (unsigned)(e >> 32), ix = (unsigned)e;
;         const bool sure = vld && (k >> 21) > bh, cand = vld && !sure;
;         const unsigned long long ms = __ballot(sure), mc = __ballot(cand);
;         const int ps = A + __builtin_popcountll(ms & ltm), pc = C + __builtin_popcountll(mc & ltm);
;         if (sure && ps < 256) LIST[ps] = (int)ix;
;         if (cand) PRIV[pc] = ((unsigned long long)k << 13) | (unsigned long long)(8191u - ix);
;         A += __builtin_popcountll(ms); C += __builtin_popcountll(mc); }
.LBB0_1231:
	s_waitcnt lgkmcnt(0)
	v_mov_b64_e32 v[0:1], v[186:187]
	ds_read_b64 v[186:187], v4 offset:512
	v_cmp_lt_u32_e64 s[0:1], s13, v3
	v_lshrrev_b32_e32 v5, 21, v1
	v_cmp_lt_u32_e32 vcc, v2, v5
	s_and_b64 s[14:15], s[0:1], vcc
	v_cndmask_b32_e64 v5, 0, 1, s[14:15]
	v_cmp_ne_u32_e32 vcc, 0, v5
	s_xor_b64 s[4:5], s[0:1], s[14:15]
	v_cndmask_b32_e64 v5, 0, 1, s[4:5]
	v_and_b32_e32 v7, vcc_lo, v34
	v_cmp_ne_u32_e64 s[0:1], 0, v5
	v_and_b32_e32 v5, vcc_hi, v33
	v_bcnt_u32_b32 v7, v7, 0
	v_bcnt_u32_b32 v5, v5, v7
	v_add_u32_e32 v5, s20, v5
	v_cmp_gt_u32_e64 s[2:3], s90, v5
	s_and_b64 s[14:15], s[14:15], s[2:3]
	s_and_saveexec_b64 s[2:3], s[14:15]
	v_lshl_add_u32 v5, v5, 2, s57
	ds_write_b32 v5, v0 offset:12288
	s_or_b64 exec, exec, s[2:3]
	s_and_saveexec_b64 s[2:3], s[4:5]
	s_cbranch_execz .LBB0_1230
	v_and_b32_e32 v7, s0, v34
	v_lshrrev_b64 v[8:9], 19, v[0:1]
	v_sub_u32_e32 v0, 0x1fff, v0
	s_movk_i32 s4, 0xe000
	v_and_b32_e32 v5, s1, v33
	v_bcnt_u32_b32 v7, v7, 0
	v_and_or_b32 v8, v8, s4, v0
	s_lshl_b32 s4, s21, 3
	v_bcnt_u32_b32 v5, v5, v7
	s_add_i32 s4, s57, s4
	v_lshl_add_u32 v0, v5, 3, s4
	ds_write_b64 v0, v[8:9]
	s_branch .LBB0_1230

; #define LAS __attribute__((address_space(3)))
; #define LDS_WAIT() asm volatile("s_waitcnt lgkmcnt(0)" ::: "memory")
; __device__ __forceinline__ bool dsa2_sampled(LAS unsigned char* wl, const unsigned (&kk)[128], int nreg, int n, int lane) {
;     ...
;         for (int lev = 0; lev < 6; ++lev) { const int w = lev < 5 ? 8 : 5; const int sh = shf - w;
;             { unsigned zq_ = 0u; asm volatile("" : "+v"(zq_)); *(LAS v4u*)(h2 + 4 * lane) = (v4u){zq_, zq_, zq_, zq_}; }
;             LDS_WAIT();
;             for (int it = 0; it < nit; ++it) { const int i = it * 64 + lane; if (i < C) { const unsigned long long c2 = PRIV[i]; if (lev == 0 || (c2 >> shf) == prefix) (void)__hip_atomic_fetch_add(&h2[(unsigned)(c2 >> sh) & ((1u << w) - 1u)], 1u, __ATOMIC_RELAXED, __HIP_MEMORY_SCOPE_WORKGROUP); } }
.LBB0_1252:
	v_mov_b32_e32 v0, v128
	s_cmp_eq_u32 s59, 5
	v_mov_b32_e32 v1, v0
	v_mov_b32_e32 v2, v0
	v_mov_b32_e32 v3, v0
	ds_write_b128 v9, v[0:3] offset:13312
	s_waitcnt lgkmcnt(0)
	s_cselect_b32 s61, 5, 8
	v_cndmask_b32_e64 v0, 0, 1, s[14:15]
	s_sub_i32 s60, s62, s61
	v_cmp_ne_u32_e64 s[0:1], 1, v0
	s_andn2_b64 vcc, exec, s[14:15]
	s_cbranch_vccnz .LBB0_1258
	s_cmp_eq_u32 s59, 0
	s_cselect_b64 s[2:3], -1, 0
	s_lshl_b32 s4, -1, s61
	s_not_b32 s63, s4
	v_mov_b32_e32 v2, v129
	v_mov_b32_e32 v3, v6
	s_mov_b32 s66, s46
	ds_read_b64 v[184:185], v3
	s_branch .LBB0_1255

; __device__ __forceinline__ bool dsa2_sampled(LAS unsigned char* wl, const unsigned (&kk)[128], int nreg, int n, int lane) {
;     ...
;             for (int it = 0; it < nit; ++it) { const int i = it * 64 + lane; if (i < C) { const unsigned long long c2 = PRIV[i]; if (lev == 0 || (c2 >> shf) == prefix) (void)__hip_atomic_fetch_add(&h2[(unsigned)(c2 >> sh) & ((1u << w) - 1u)], 1u, __ATOMIC_RELAXED, __HIP_MEMORY_SCOPE_WORKGROUP); } }
.LBB0_1255:
	s_waitcnt lgkmcnt(0)
	v_mov_b64_e32 v[0:1], v[184:185]
	ds_read_b64 v[184:185], v3 offset:512
	v_cmp_gt_u32_e32 vcc, s21, v2
	s_and_saveexec_b64 s[4:5], vcc
	s_cbranch_execz .LBB0_1254
	v_lshrrev_b64 v[10:11], s62, v[0:1]
	v_cmp_eq_u64_e32 vcc, v[10:11], v[4:5]
	s_or_b64 s[42:43], s[2:3], vcc
	s_and_b64 exec, exec, s[42:43]
	s_cbranch_execz .LBB0_1254
	v_lshrrev_b64 v[0:1], s60, v[0:1]
	v_and_b32_e32 v0, s63, v0
	v_lshl_add_u32 v0, v0, 2, s57
	ds_add_u32 v0, v248 offset:13312
	s_branch .LBB0_1254

; __device__ __forceinline__ bool dsa2_sampled(LAS unsigned char* wl, const unsigned (&kk)[128], int nreg, int n, int lane) {
;     ...
;         int pos = A;
;         for (int it = 0; it < nit; ++it) { const int i = it * 64 + lane; unsigned long long c2 = 0ull; if (i < C) c2 = PRIV[i];
;             const bool take = (i < C) && ((c2 >> shf) >= prefix);
.LBB0_1263:
	s_or_b64 exec, exec, s[12:13]
	s_and_b64 vcc, exec, s[0:1]
	s_mov_b32 s62, s84
	s_cbranch_vccnz .LBB0_1270
	v_mov_b32_e32 v1, v129
	ds_read_b64 v[184:185], v6
	s_branch .LBB0_1266

; __device__ __forceinline__ bool dsa2_sampled(LAS unsigned char* wl, const unsigned (&kk)[128], int nreg, int n, int lane) {
;     ...
;         for (int it = 0; it < nit; ++it) { const int i = it * 64 + lane; unsigned long long c2 = 0ull; if (i < C) c2 = PRIV[i];
;             const bool take = (i < C) && ((c2 >> shf) >= prefix);
;             const unsigned long long mt = __ballot(take);
;             if (take) LIST[pos + __builtin_popcountll(mt & ltm)] = (int)(8191u - (unsigned)(c2 & 8191ull));
;             pos += __builtin_popcountll(mt); }
.LBB0_1266:
	s_waitcnt lgkmcnt(0)
	v_mov_b64_e32 v[2:3], v[184:185]
	ds_read_b64 v[184:185], v6 offset:512
	v_cmp_gt_u32_e32 vcc, s21, v1
	v_lshrrev_b64 v[8:9], v0, v[2:3]
	v_cmp_ge_u64_e64 s[0:1], v[8:9], v[4:5]
	s_and_b64 s[2:3], vcc, s[0:1]
	v_cndmask_b32_e64 v3, 0, 1, s[2:3]
	v_cmp_ne_u32_e32 vcc, 0, v3
	s_and_saveexec_b64 s[0:1], s[2:3]
	s_cbranch_execz .LBB0_1265
	v_and_b32_e32 v7, vcc_lo, v34
	s_lshl_b32 s2, s20, 2
	v_and_b32_e32 v3, vcc_hi, v33
	v_bcnt_u32_b32 v7, v7, 0
	s_add_i32 s2, s57, s2
	v_bcnt_u32_b32 v3, v3, v7
	v_lshl_add_u32 v3, v3, 2, s2
	s_movk_i32 s2, 0x1fff
	v_bitop3_b32 v2, v2, s2, v2 bitop3:0xc
	ds_write_b32 v3, v2 offset:12288
	s_branch .LBB0_1265
